# P4 softmax epilogue: per-row ssq statistics loads issued three rows ahead into rotating buffers (counted vmcnt) instead of one exposed latency per row
# baseline (speedup 1.0000x reference)
; __device__ __forceinline__ float row_rms_from_ssq(const float* ssq, int row) {
;     const f32x4* p = (const f32x4*)(ssq + (size_t)row * 16); const f32x4 a = p[0], b = p[1], c = p[2], d = p[3];
;     const float s = (((a[0] + a[1]) + (a[2] + a[3])) + ((b[0] + b[1]) + (b[2] + b[3]))) + (((c[0] + c[1]) + (c[2] + c[3])) + ((d[0] + d[1]) + (d[2] + d[3])));
;     return rsqrtf(s * (1.0f / D) + EPS);
;     __device__ __forceinline__ void operator()(f32x4 (&acc)[2][2][4][2], const pg8::Unit& u, int wr, int wc, int fr, int fq) const {
;     ...
;                 const float r = row_rms_from_ssq(ssq, row0 + ai * 128 + m * 16) * (1.4426950408889634f / 64.0f);
;                 float mm = -3.0e38f;
; #pragma unroll
;                 for (int bj = 0; bj < 2; ++bj)
; #pragma unroll
;                     for (int n = 0; n < 2; ++n) { acc[ai][bj][m][n] = acc[ai][bj][m][n] * r; const f32x4 v = acc[ai][bj][m][n]; mm = fmaxf(fmaxf(fmaxf(mm, v[0]), fmaxf(v[1], v[2])), v[3]); }
;                 mm = fmaxf(mm, __shfl_xor(mm, 16)); mm = fmaxf(mm, __shfl_xor(mm, 32));
;                 if (fq == 0) xch[(ai * 128 + wr * 64 + m * 16 + fr) * 4 + wc] = mm; }
.LBB0_648:
	v_mov_b32_e32 v131, v0
	s_lshl_b32 s2, s41, 8
	s_add_i32 s2, s2, s34
	v_and_b32_e32 v152, 15, v131
	v_or_b32_e32 v132, s2, v152
	v_ashrrev_i32_e32 v133, 31, v132
	v_lshlrev_b64 v[134:135], 6, v[132:133]
	v_lshl_add_u64 v[146:147], s[20:21], 0, v[134:135]
	s_mov_b64 s[98:99], 0x2000
	v_mov_b64_e32 v[174:175], v[146:147]
	global_load_dwordx4 v[206:209], v[174:175], off
	global_load_dwordx4 v[210:213], v[174:175], off offset:16
	global_load_dwordx4 v[214:217], v[174:175], off offset:32
	global_load_dwordx4 v[218:221], v[174:175], off offset:48
	global_load_dwordx4 v[222:225], v[174:175], off offset:1024
	global_load_dwordx4 v[226:229], v[174:175], off offset:1040
	global_load_dwordx4 v[230:233], v[174:175], off offset:1056
	global_load_dwordx4 v[234:237], v[174:175], off offset:1072
	global_load_dwordx4 v[238:241], v[174:175], off offset:2048
	global_load_dwordx4 v[242:245], v[174:175], off offset:2064
	global_load_dwordx4 v[246:249], v[174:175], off offset:2080
	global_load_dwordx4 v[250:253], v[174:175], off offset:2096
	s_waitcnt vmcnt(8)
	v_mov_b64_e32 v[134:135], v[206:207]
	v_mov_b64_e32 v[136:137], v[208:209]
	v_mov_b64_e32 v[138:139], v[214:215]
	v_mov_b64_e32 v[140:141], v[216:217]
	v_mov_b64_e32 v[142:143], v[210:211]
	v_mov_b64_e32 v[144:145], v[212:213]
	v_mov_b64_e32 v[146:147], v[218:219]
	v_mov_b64_e32 v[148:149], v[220:221]
	global_load_dwordx4 v[206:209], v[174:175], off offset:3072
	global_load_dwordx4 v[210:213], v[174:175], off offset:3088
	global_load_dwordx4 v[214:217], v[174:175], off offset:3104
	global_load_dwordx4 v[218:221], v[174:175], off offset:3120
	v_and_b32_e32 v150, 64, v200
	v_add_u32_e32 v154, 64, v150
	v_xor_b32_e32 v153, 16, v200
	v_cmp_lt_i32_e64 s[2:3], v153, v154
	v_bfe_u32 v131, v131, 4, 2
	v_or_b32_e32 v164, s34, v152
	v_lshl_add_u32 v165, v164, 4, s36
	v_mov_b32_e32 v150, v134
	v_mov_b32_e32 v151, v138
	v_mov_b32_e32 v138, v135
	v_mov_b32_e32 v134, v136
	v_mov_b32_e32 v135, v140
	v_mov_b32_e32 v140, v137
	v_mov_b32_e32 v136, v142
	v_mov_b32_e32 v137, v146
	v_mov_b32_e32 v146, v143
	v_mov_b32_e32 v142, v144
	v_mov_b32_e32 v143, v148
	v_mov_b32_e32 v148, v145
	v_pk_add_f32 v[138:139], v[150:151], v[138:139]
	v_pk_add_f32 v[134:135], v[134:135], v[140:141]
	v_pk_add_f32 v[136:137], v[136:137], v[146:147]
	v_pk_add_f32 v[140:141], v[142:143], v[148:149]
	v_pk_add_f32 v[134:135], v[138:139], v[134:135]
	v_pk_add_f32 v[136:137], v[136:137], v[140:141]
	s_nop 0
	v_pk_add_f32 v[134:135], v[134:135], v[136:137]
	s_nop 0
	v_add_f32_e32 v134, v134, v135
	v_fmamk_f32 v134, v134, 0x3a800000, v199
	v_mul_f32_e32 v135, 0x4b800000, v134
	v_cmp_gt_f32_e32 vcc, s37, v134
	s_nop 1
	v_cndmask_b32_e32 v134, v134, v135, vcc
	v_rsq_f32_e32 v134, v134
	v_cndmask_b32_e64 v135, v200, v153, s[2:3]
	v_lshlrev_b32_e32 v201, 2, v135
	v_cmp_ne_u32_e64 s[2:3], 0, v131
	v_mul_f32_e32 v135, 0x45800000, v134
	v_cndmask_b32_e32 v134, v134, v135, vcc
	v_mul_f32_e32 v142, 0x3cb8aa3b, v134
	v_pk_mul_f32 v[138:139], v[116:117], v[142:143] op_sel_hi:[1,0]
	v_pk_mul_f32 v[140:141], v[114:115], v[142:143] op_sel_hi:[1,0]
	v_pk_mul_f32 v[134:135], v[120:121], v[142:143] op_sel_hi:[1,0]
	v_max_f32_e32 v114, v141, v138
	v_pk_mul_f32 v[136:137], v[118:119], v[142:143] op_sel_hi:[1,0]
	v_max3_f32 v114, v140, s38, v114
	v_pk_mul_f32 v[120:121], v[124:125], v[142:143] op_sel_hi:[1,0]
	v_pk_mul_f32 v[122:123], v[122:123], v[142:143] op_sel_hi:[1,0]
	v_max_f32_e32 v115, v137, v134
	v_max3_f32 v114, v114, v139, v136
	v_max_f32_e32 v124, v123, v120
	v_max3_f32 v114, v114, v115, v135
	v_pk_mul_f32 v[116:117], v[128:129], v[142:143] op_sel_hi:[1,0]
	v_pk_mul_f32 v[118:119], v[126:127], v[142:143] op_sel_hi:[1,0]
	v_max3_f32 v114, v114, v122, v124
	v_max_f32_e32 v125, v119, v116
	v_max3_f32 v114, v114, v121, v118
	v_max3_f32 v114, v114, v125, v117
	ds_bpermute_b32 v115, v201, v114
	v_xor_b32_e32 v124, 32, v200
	v_cmp_lt_i32_e32 vcc, v124, v154
	s_waitcnt lgkmcnt(0)
	v_max_f32_e32 v115, v115, v115
	v_cndmask_b32_e32 v124, v200, v124, vcc
	v_max_f32_e32 v114, v114, v115
	v_lshlrev_b32_e32 v202, 2, v124
	ds_bpermute_b32 v115, v202, v114
	v_cmp_eq_u32_e32 vcc, 0, v131
	s_and_saveexec_b64 s[4:5], vcc
	s_cbranch_execz .LBB0_650
	s_waitcnt lgkmcnt(0)
	v_max_f32_e32 v115, v115, v115
	v_max_f32_e32 v114, v114, v114
	v_max_f32_e32 v114, v114, v115
	ds_write_b32 v165, v114
; __device__ __forceinline__ float row_rms_from_ssq(const float* ssq, int row) {
;     const f32x4* p = (const f32x4*)(ssq + (size_t)row * 16); const f32x4 a = p[0], b = p[1], c = p[2], d = p[3];
;     const float s = (((a[0] + a[1]) + (a[2] + a[3])) + ((b[0] + b[1]) + (b[2] + b[3]))) + (((c[0] + c[1]) + (c[2] + c[3])) + ((d[0] + d[1]) + (d[2] + d[3])));
;     return rsqrtf(s * (1.0f / D) + EPS);
;     __device__ __forceinline__ void operator()(f32x4 (&acc)[2][2][4][2], const pg8::Unit& u, int wr, int wc, int fr, int fq) const {
;     ...
;                 const float r = row_rms_from_ssq(ssq, row0 + ai * 128 + m * 16) * (1.4426950408889634f / 64.0f);
;                 float mm = -3.0e38f;
; #pragma unroll
;                 for (int bj = 0; bj < 2; ++bj)
; #pragma unroll
;                     for (int n = 0; n < 2; ++n) { acc[ai][bj][m][n] = acc[ai][bj][m][n] * r; const f32x4 v = acc[ai][bj][m][n]; mm = fmaxf(fmaxf(fmaxf(mm, v[0]), fmaxf(v[1], v[2])), v[3]); }
;                 mm = fmaxf(mm, __shfl_xor(mm, 16)); mm = fmaxf(mm, __shfl_xor(mm, 32));
;                 if (fq == 0) xch[(ai * 128 + wr * 64 + m * 16 + fr) * 4 + wc] = mm; }
.LBB0_650:
	s_or_b64 exec, exec, s[4:5]
	v_or_b32_e32 v114, 16, v132
	s_waitcnt lgkmcnt(0)
	v_ashrrev_i32_e32 v115, 31, v114
	v_lshlrev_b64 v[124:125], 6, v[114:115]
	v_lshl_add_u64 v[128:129], s[20:21], 0, v[124:125]
	s_waitcnt vmcnt(8)
	v_mov_b64_e32 v[124:125], v[222:223]
	v_mov_b64_e32 v[126:127], v[224:225]
	v_mov_b64_e32 v[142:143], v[230:231]
	v_mov_b64_e32 v[144:145], v[232:233]
	v_mov_b64_e32 v[146:147], v[226:227]
	v_mov_b64_e32 v[148:149], v[228:229]
	v_mov_b64_e32 v[150:151], v[234:235]
	v_mov_b64_e32 v[152:153], v[236:237]
	v_lshl_add_u64 v[174:175], v[174:175], 0, s[98:99]
	global_load_dwordx4 v[222:225], v[174:175], off
	global_load_dwordx4 v[226:229], v[174:175], off offset:16
	global_load_dwordx4 v[230:233], v[174:175], off offset:32
	global_load_dwordx4 v[234:237], v[174:175], off offset:48
	v_mov_b32_e32 v128, v124
	v_mov_b32_e32 v129, v142
	v_mov_b32_e32 v142, v125
	v_mov_b32_e32 v124, v126
	v_mov_b32_e32 v125, v144
	v_mov_b32_e32 v144, v127
	v_mov_b32_e32 v126, v146
	v_mov_b32_e32 v127, v150
	v_mov_b32_e32 v150, v147
	v_mov_b32_e32 v146, v148
	v_mov_b32_e32 v147, v152
	v_mov_b32_e32 v152, v149
	v_pk_add_f32 v[128:129], v[128:129], v[142:143]
	v_pk_add_f32 v[124:125], v[124:125], v[144:145]
	v_pk_add_f32 v[126:127], v[126:127], v[150:151]
	v_pk_add_f32 v[142:143], v[146:147], v[152:153]
	v_pk_add_f32 v[124:125], v[128:129], v[124:125]
	v_pk_add_f32 v[126:127], v[126:127], v[142:143]
	s_nop 0
	v_pk_add_f32 v[124:125], v[124:125], v[126:127]
	s_nop 0
	v_add_f32_e32 v124, v124, v125
	v_fmamk_f32 v124, v124, 0x3a800000, v199
	v_mul_f32_e32 v125, 0x4b800000, v124
	v_cmp_gt_f32_e64 s[4:5], s37, v124
	s_nop 1
	v_cndmask_b32_e64 v124, v124, v125, s[4:5]
	v_rsq_f32_e32 v124, v124
	s_nop 0
	v_mul_f32_e32 v125, 0x45800000, v124
	v_cndmask_b32_e64 v124, v124, v125, s[4:5]
	v_mul_f32_e32 v144, 0x3cb8aa3b, v124
	v_pk_mul_f32 v[128:129], v[104:105], v[144:145] op_sel_hi:[1,0]
	v_pk_mul_f32 v[142:143], v[102:103], v[144:145] op_sel_hi:[1,0]
	v_pk_mul_f32 v[126:127], v[98:99], v[144:145] op_sel_hi:[1,0]
	v_max_f32_e32 v98, v143, v128
	v_pk_mul_f32 v[124:125], v[100:101], v[144:145] op_sel_hi:[1,0]
	v_max3_f32 v98, v142, s38, v98
	v_pk_mul_f32 v[104:105], v[112:113], v[144:145] op_sel_hi:[1,0]
	v_pk_mul_f32 v[110:111], v[110:111], v[144:145] op_sel_hi:[1,0]
	v_max_f32_e32 v99, v127, v124
	v_max3_f32 v98, v98, v129, v126
	v_pk_mul_f32 v[102:103], v[106:107], v[144:145] op_sel_hi:[1,0]
	v_max_f32_e32 v106, v111, v104
	v_max3_f32 v98, v98, v99, v125
	v_pk_mul_f32 v[100:101], v[108:109], v[144:145] op_sel_hi:[1,0]
	v_max3_f32 v98, v98, v110, v106
	v_max3_f32 v98, v98, v105, v102
	v_max_f32_e32 v99, v103, v100
	v_max3_f32 v98, v98, v99, v101
	ds_bpermute_b32 v99, v201, v98
	s_waitcnt lgkmcnt(0)
	v_max_f32_e32 v99, v99, v99
	v_max_f32_e32 v98, v98, v99
	ds_bpermute_b32 v99, v202, v98
	s_and_saveexec_b64 s[4:5], vcc
	s_cbranch_execz .LBB0_652
	s_waitcnt lgkmcnt(0)
	v_max_f32_e32 v99, v99, v99
	v_max_f32_e32 v98, v98, v98
	v_max_f32_e32 v98, v98, v99
	ds_write_b32 v165, v98 offset:256
.LBB0_652:
	s_or_b64 exec, exec, s[4:5]
	v_or_b32_e32 v98, 32, v132
	s_waitcnt lgkmcnt(0)
	v_ashrrev_i32_e32 v99, 31, v98
	v_lshlrev_b64 v[106:107], 6, v[98:99]
	v_lshl_add_u64 v[112:113], s[20:21], 0, v[106:107]
	s_waitcnt vmcnt(8)
	v_mov_b64_e32 v[106:107], v[238:239]
	v_mov_b64_e32 v[108:109], v[240:241]
	v_mov_b64_e32 v[144:145], v[246:247]
	v_mov_b64_e32 v[146:147], v[248:249]
	v_mov_b64_e32 v[148:149], v[242:243]
	v_mov_b64_e32 v[150:151], v[244:245]
	v_mov_b64_e32 v[152:153], v[250:251]
	v_mov_b64_e32 v[154:155], v[252:253]
	global_load_dwordx4 v[238:241], v[174:175], off offset:1024
	global_load_dwordx4 v[242:245], v[174:175], off offset:1040
	global_load_dwordx4 v[246:249], v[174:175], off offset:1056
	global_load_dwordx4 v[250:253], v[174:175], off offset:1072
	v_mov_b32_e32 v112, v106
	v_mov_b32_e32 v113, v144
	v_mov_b32_e32 v144, v107
	v_mov_b32_e32 v106, v108
	v_mov_b32_e32 v107, v146
	v_mov_b32_e32 v146, v109
	v_mov_b32_e32 v108, v148
	v_mov_b32_e32 v109, v152
	v_mov_b32_e32 v152, v149
	v_mov_b32_e32 v148, v150
	v_mov_b32_e32 v149, v154
	v_mov_b32_e32 v154, v151
	v_pk_add_f32 v[112:113], v[112:113], v[144:145]
	v_pk_add_f32 v[106:107], v[106:107], v[146:147]
	v_pk_add_f32 v[108:109], v[108:109], v[152:153]
	v_pk_add_f32 v[144:145], v[148:149], v[154:155]
	v_pk_add_f32 v[106:107], v[112:113], v[106:107]
	v_pk_add_f32 v[108:109], v[108:109], v[144:145]
	s_nop 0
	v_pk_add_f32 v[106:107], v[106:107], v[108:109]
	s_nop 0
	v_add_f32_e32 v106, v106, v107
	v_fmamk_f32 v106, v106, 0x3a800000, v199
	v_mul_f32_e32 v107, 0x4b800000, v106
	v_cmp_gt_f32_e64 s[4:5], s37, v106
	s_nop 1
	v_cndmask_b32_e64 v106, v106, v107, s[4:5]
	v_rsq_f32_e32 v106, v106
	s_nop 0
	v_mul_f32_e32 v107, 0x45800000, v106
	v_cndmask_b32_e64 v106, v106, v107, s[4:5]
	v_mul_f32_e32 v146, 0x3cb8aa3b, v106
	v_pk_mul_f32 v[112:113], v[88:89], v[146:147] op_sel_hi:[1,0]
	v_pk_mul_f32 v[144:145], v[86:87], v[146:147] op_sel_hi:[1,0]
	v_pk_mul_f32 v[108:109], v[82:83], v[146:147] op_sel_hi:[1,0]
	v_max_f32_e32 v82, v145, v112
	v_pk_mul_f32 v[106:107], v[84:85], v[146:147] op_sel_hi:[1,0]
	v_max3_f32 v82, v144, s38, v82
	v_pk_mul_f32 v[88:89], v[96:97], v[146:147] op_sel_hi:[1,0]
	v_pk_mul_f32 v[94:95], v[94:95], v[146:147] op_sel_hi:[1,0]
	v_max_f32_e32 v83, v109, v106
	v_max3_f32 v82, v82, v113, v108
	v_pk_mul_f32 v[86:87], v[90:91], v[146:147] op_sel_hi:[1,0]
	v_max_f32_e32 v90, v95, v88
	v_max3_f32 v82, v82, v83, v107
	v_pk_mul_f32 v[84:85], v[92:93], v[146:147] op_sel_hi:[1,0]
	v_max3_f32 v82, v82, v94, v90
	v_max3_f32 v82, v82, v89, v86
	v_max_f32_e32 v83, v87, v84
	v_max3_f32 v82, v82, v83, v85
	ds_bpermute_b32 v83, v201, v82
	s_waitcnt lgkmcnt(0)
	v_max_f32_e32 v83, v83, v83
	v_max_f32_e32 v82, v82, v83
	ds_bpermute_b32 v83, v202, v82
	s_and_saveexec_b64 s[4:5], vcc
	s_cbranch_execz .LBB0_654
	s_waitcnt lgkmcnt(0)
	v_max_f32_e32 v83, v83, v83
	v_max_f32_e32 v82, v82, v82
	v_max_f32_e32 v82, v82, v83
	ds_write_b32 v165, v82 offset:512
; __device__ __forceinline__ float row_rms_from_ssq(const float* ssq, int row) {
;     const f32x4* p = (const f32x4*)(ssq + (size_t)row * 16); const f32x4 a = p[0], b = p[1], c = p[2], d = p[3];
;     const float s = (((a[0] + a[1]) + (a[2] + a[3])) + ((b[0] + b[1]) + (b[2] + b[3]))) + (((c[0] + c[1]) + (c[2] + c[3])) + ((d[0] + d[1]) + (d[2] + d[3])));
;     return rsqrtf(s * (1.0f / D) + EPS);
;     __device__ __forceinline__ void operator()(f32x4 (&acc)[2][2][4][2], const pg8::Unit& u, int wr, int wc, int fr, int fq) const {
;     ...
;                 const float r = row_rms_from_ssq(ssq, row0 + ai * 128 + m * 16) * (1.4426950408889634f / 64.0f);
;                 float mm = -3.0e38f;
; #pragma unroll
;                 for (int bj = 0; bj < 2; ++bj)
; #pragma unroll
;                     for (int n = 0; n < 2; ++n) { acc[ai][bj][m][n] = acc[ai][bj][m][n] * r; const f32x4 v = acc[ai][bj][m][n]; mm = fmaxf(fmaxf(fmaxf(mm, v[0]), fmaxf(v[1], v[2])), v[3]); }
;                 mm = fmaxf(mm, __shfl_xor(mm, 16)); mm = fmaxf(mm, __shfl_xor(mm, 32));
;                 if (fq == 0) xch[(ai * 128 + wr * 64 + m * 16 + fr) * 4 + wc] = mm; }
.LBB0_654:
	s_or_b64 exec, exec, s[4:5]
	v_or_b32_e32 v82, 48, v132
	s_waitcnt lgkmcnt(0)
	v_ashrrev_i32_e32 v83, 31, v82
	v_lshlrev_b64 v[90:91], 6, v[82:83]
	v_lshl_add_u64 v[96:97], s[20:21], 0, v[90:91]
	s_waitcnt vmcnt(8)
	v_mov_b64_e32 v[90:91], v[206:207]
	v_mov_b64_e32 v[92:93], v[208:209]
	v_mov_b64_e32 v[146:147], v[214:215]
	v_mov_b64_e32 v[148:149], v[216:217]
	v_mov_b64_e32 v[150:151], v[210:211]
	v_mov_b64_e32 v[152:153], v[212:213]
	v_mov_b64_e32 v[154:155], v[218:219]
	v_mov_b64_e32 v[156:157], v[220:221]
	global_load_dwordx4 v[206:209], v[174:175], off offset:2048
	global_load_dwordx4 v[210:213], v[174:175], off offset:2064
	global_load_dwordx4 v[214:217], v[174:175], off offset:2080
	global_load_dwordx4 v[218:221], v[174:175], off offset:2096
	v_mov_b32_e32 v96, v90
	v_mov_b32_e32 v97, v146
	v_mov_b32_e32 v146, v91
	v_mov_b32_e32 v90, v92
	v_mov_b32_e32 v91, v148
	v_mov_b32_e32 v148, v93
	v_mov_b32_e32 v92, v150
	v_mov_b32_e32 v93, v154
	v_mov_b32_e32 v154, v151
	v_mov_b32_e32 v150, v152
	v_mov_b32_e32 v151, v156
	v_mov_b32_e32 v156, v153
	v_pk_add_f32 v[96:97], v[96:97], v[146:147]
	v_pk_add_f32 v[90:91], v[90:91], v[148:149]
	v_pk_add_f32 v[92:93], v[92:93], v[154:155]
	v_pk_add_f32 v[146:147], v[150:151], v[156:157]
	v_pk_add_f32 v[90:91], v[96:97], v[90:91]
	v_pk_add_f32 v[92:93], v[92:93], v[146:147]
	s_nop 0
	v_pk_add_f32 v[90:91], v[90:91], v[92:93]
	s_nop 0
	v_add_f32_e32 v90, v90, v91
	v_fmamk_f32 v90, v90, 0x3a800000, v199
	v_mul_f32_e32 v91, 0x4b800000, v90
	v_cmp_gt_f32_e64 s[4:5], s37, v90
	s_nop 1
	v_cndmask_b32_e64 v90, v90, v91, s[4:5]
	v_rsq_f32_e32 v90, v90
	s_nop 0
	v_mul_f32_e32 v91, 0x45800000, v90
	v_cndmask_b32_e64 v90, v90, v91, s[4:5]
	v_mul_f32_e32 v148, 0x3cb8aa3b, v90
	v_pk_mul_f32 v[96:97], v[72:73], v[148:149] op_sel_hi:[1,0]
	v_pk_mul_f32 v[146:147], v[70:71], v[148:149] op_sel_hi:[1,0]
	v_pk_mul_f32 v[92:93], v[66:67], v[148:149] op_sel_hi:[1,0]
	v_max_f32_e32 v66, v147, v96
	v_pk_mul_f32 v[90:91], v[68:69], v[148:149] op_sel_hi:[1,0]
	v_max3_f32 v66, v146, s38, v66
	v_pk_mul_f32 v[72:73], v[80:81], v[148:149] op_sel_hi:[1,0]
	v_pk_mul_f32 v[78:79], v[78:79], v[148:149] op_sel_hi:[1,0]
	v_max_f32_e32 v67, v93, v90
	v_max3_f32 v66, v66, v97, v92
	v_pk_mul_f32 v[70:71], v[74:75], v[148:149] op_sel_hi:[1,0]
	v_max_f32_e32 v74, v79, v72
	v_max3_f32 v66, v66, v67, v91
	v_pk_mul_f32 v[68:69], v[76:77], v[148:149] op_sel_hi:[1,0]
	v_max3_f32 v66, v66, v78, v74
	v_max3_f32 v66, v66, v73, v70
	v_max_f32_e32 v67, v71, v68
	v_max3_f32 v66, v66, v67, v69
	ds_bpermute_b32 v67, v201, v66
	s_waitcnt lgkmcnt(0)
	v_max_f32_e32 v67, v67, v67
	v_max_f32_e32 v66, v66, v67
	ds_bpermute_b32 v67, v202, v66
	s_and_saveexec_b64 s[4:5], vcc
	s_cbranch_execz .LBB0_656
	s_waitcnt lgkmcnt(0)
	v_max_f32_e32 v67, v67, v67
	v_max_f32_e32 v66, v66, v66
	v_max_f32_e32 v66, v66, v67
	ds_write_b32 v165, v66 offset:768
.LBB0_656:
	s_or_b64 exec, exec, s[4:5]
	v_add_u32_e32 v66, 0x80, v132
	s_waitcnt lgkmcnt(0)
	v_ashrrev_i32_e32 v67, 31, v66
	v_lshlrev_b64 v[74:75], 6, v[66:67]
	v_lshl_add_u64 v[80:81], s[20:21], 0, v[74:75]
	s_waitcnt vmcnt(8)
	v_mov_b64_e32 v[74:75], v[222:223]
	v_mov_b64_e32 v[76:77], v[224:225]
	v_mov_b64_e32 v[148:149], v[230:231]
	v_mov_b64_e32 v[150:151], v[232:233]
	v_mov_b64_e32 v[152:153], v[226:227]
	v_mov_b64_e32 v[154:155], v[228:229]
	v_mov_b64_e32 v[156:157], v[234:235]
	v_mov_b64_e32 v[158:159], v[236:237]
	global_load_dwordx4 v[222:225], v[174:175], off offset:3072
	global_load_dwordx4 v[226:229], v[174:175], off offset:3088
	global_load_dwordx4 v[230:233], v[174:175], off offset:3104
	global_load_dwordx4 v[234:237], v[174:175], off offset:3120
	v_add_u32_e32 v203, 0x80, v164
	v_mov_b32_e32 v80, v74
	v_mov_b32_e32 v81, v148
	v_mov_b32_e32 v148, v75
	v_mov_b32_e32 v74, v76
	v_mov_b32_e32 v75, v150
	v_mov_b32_e32 v150, v77
	v_mov_b32_e32 v76, v152
	v_mov_b32_e32 v77, v156
	v_mov_b32_e32 v156, v153
	v_mov_b32_e32 v152, v154
	v_mov_b32_e32 v153, v158
	v_mov_b32_e32 v158, v155
	v_pk_add_f32 v[80:81], v[80:81], v[148:149]
	v_pk_add_f32 v[74:75], v[74:75], v[150:151]
	v_pk_add_f32 v[76:77], v[76:77], v[156:157]
	v_pk_add_f32 v[148:149], v[152:153], v[158:159]
	v_pk_add_f32 v[74:75], v[80:81], v[74:75]
	v_pk_add_f32 v[76:77], v[76:77], v[148:149]
	s_nop 0
	v_pk_add_f32 v[74:75], v[74:75], v[76:77]
	s_nop 0
	v_add_f32_e32 v74, v74, v75
	v_fmamk_f32 v74, v74, 0x3a800000, v199
	v_mul_f32_e32 v75, 0x4b800000, v74
	v_cmp_gt_f32_e64 s[4:5], s37, v74
	s_nop 1
	v_cndmask_b32_e64 v74, v74, v75, s[4:5]
	v_rsq_f32_e32 v74, v74
	s_nop 0
	v_mul_f32_e32 v75, 0x45800000, v74
	v_cndmask_b32_e64 v74, v74, v75, s[4:5]
	v_mul_f32_e32 v74, 0x3cb8aa3b, v74
	v_pk_mul_f32 v[152:153], v[56:57], v[74:75] op_sel_hi:[1,0]
	v_pk_mul_f32 v[154:155], v[54:55], v[74:75] op_sel_hi:[1,0]
	v_pk_mul_f32 v[150:151], v[50:51], v[74:75] op_sel_hi:[1,0]
	v_max_f32_e32 v50, v155, v152
	v_pk_mul_f32 v[148:149], v[52:53], v[74:75] op_sel_hi:[1,0]
	v_max3_f32 v50, v154, s38, v50
	v_pk_mul_f32 v[56:57], v[64:65], v[74:75] op_sel_hi:[1,0]
	v_pk_mul_f32 v[64:65], v[62:63], v[74:75] op_sel_hi:[1,0]
	v_max_f32_e32 v51, v151, v148
	v_max3_f32 v50, v50, v153, v150
	v_pk_mul_f32 v[54:55], v[58:59], v[74:75] op_sel_hi:[1,0]
	v_max_f32_e32 v58, v65, v56
	v_max3_f32 v50, v50, v51, v149
	v_pk_mul_f32 v[52:53], v[60:61], v[74:75] op_sel_hi:[1,0]
	v_max3_f32 v50, v50, v64, v58
	v_max3_f32 v50, v50, v57, v54
	v_max_f32_e32 v51, v55, v52
	v_max3_f32 v50, v50, v51, v53
	ds_bpermute_b32 v51, v201, v50
	s_waitcnt lgkmcnt(0)
	v_max_f32_e32 v51, v51, v51
	v_max_f32_e32 v50, v50, v51
	ds_bpermute_b32 v51, v202, v50
	s_and_saveexec_b64 s[4:5], vcc
	s_cbranch_execz .LBB0_658
	s_waitcnt lgkmcnt(0)
	v_max_f32_e32 v51, v51, v51
	v_max_f32_e32 v50, v50, v50
	v_lshl_add_u32 v58, v203, 4, s36
	v_max_f32_e32 v50, v50, v51
	ds_write_b32 v58, v50
; __device__ __forceinline__ float row_rms_from_ssq(const float* ssq, int row) {
;     const f32x4* p = (const f32x4*)(ssq + (size_t)row * 16); const f32x4 a = p[0], b = p[1], c = p[2], d = p[3];
;     const float s = (((a[0] + a[1]) + (a[2] + a[3])) + ((b[0] + b[1]) + (b[2] + b[3]))) + (((c[0] + c[1]) + (c[2] + c[3])) + ((d[0] + d[1]) + (d[2] + d[3])));
;     return rsqrtf(s * (1.0f / D) + EPS);
;     __device__ __forceinline__ void operator()(f32x4 (&acc)[2][2][4][2], const pg8::Unit& u, int wr, int wc, int fr, int fq) const {
;     ...
;                 const float r = row_rms_from_ssq(ssq, row0 + ai * 128 + m * 16) * (1.4426950408889634f / 64.0f);
;                 float mm = -3.0e38f;
; #pragma unroll
;                 for (int bj = 0; bj < 2; ++bj)
; #pragma unroll
;                     for (int n = 0; n < 2; ++n) { acc[ai][bj][m][n] = acc[ai][bj][m][n] * r; const f32x4 v = acc[ai][bj][m][n]; mm = fmaxf(fmaxf(fmaxf(mm, v[0]), fmaxf(v[1], v[2])), v[3]); }
;                 mm = fmaxf(mm, __shfl_xor(mm, 16)); mm = fmaxf(mm, __shfl_xor(mm, 32));
;                 if (fq == 0) xch[(ai * 128 + wr * 64 + m * 16 + fr) * 4 + wc] = mm; }
.LBB0_658:
	s_or_b64 exec, exec, s[4:5]
	v_add_u32_e32 v50, 0x90, v132
	s_waitcnt lgkmcnt(0)
	v_ashrrev_i32_e32 v51, 31, v50
	v_lshlrev_b64 v[58:59], 6, v[50:51]
	v_lshl_add_u64 v[62:63], s[20:21], 0, v[58:59]
	s_waitcnt vmcnt(8)
	v_mov_b64_e32 v[58:59], v[238:239]
	v_mov_b64_e32 v[60:61], v[240:241]
	v_mov_b64_e32 v[74:75], v[246:247]
	v_mov_b64_e32 v[76:77], v[248:249]
	v_mov_b64_e32 v[156:157], v[242:243]
	v_mov_b64_e32 v[158:159], v[244:245]
	v_mov_b64_e32 v[160:161], v[250:251]
	v_mov_b64_e32 v[162:163], v[252:253]
	v_mov_b32_e32 v62, v58
	v_mov_b32_e32 v63, v74
	v_mov_b32_e32 v74, v59
	v_mov_b32_e32 v58, v60
	v_mov_b32_e32 v59, v76
	v_mov_b32_e32 v76, v61
	v_mov_b32_e32 v60, v156
	v_mov_b32_e32 v61, v160
	v_mov_b32_e32 v160, v157
	v_mov_b32_e32 v80, v158
	v_mov_b32_e32 v81, v162
	v_mov_b32_e32 v162, v159
	v_pk_add_f32 v[62:63], v[62:63], v[74:75]
	v_pk_add_f32 v[58:59], v[58:59], v[76:77]
	v_pk_add_f32 v[60:61], v[60:61], v[160:161]
	v_pk_add_f32 v[74:75], v[80:81], v[162:163]
	v_pk_add_f32 v[58:59], v[62:63], v[58:59]
	v_pk_add_f32 v[60:61], v[60:61], v[74:75]
	s_nop 0
	v_pk_add_f32 v[58:59], v[58:59], v[60:61]
	s_nop 0
	v_add_f32_e32 v58, v58, v59
	v_fmamk_f32 v58, v58, 0x3a800000, v199
	v_mul_f32_e32 v59, 0x4b800000, v58
	v_cmp_gt_f32_e64 s[4:5], s37, v58
	s_nop 1
	v_cndmask_b32_e64 v58, v58, v59, s[4:5]
	v_rsq_f32_e32 v58, v58
	s_nop 0
	v_mul_f32_e32 v59, 0x45800000, v58
	v_cndmask_b32_e64 v58, v58, v59, s[4:5]
	v_mul_f32_e32 v58, 0x3cb8aa3b, v58
	v_pk_mul_f32 v[60:61], v[40:41], v[58:59] op_sel_hi:[1,0]
	v_pk_mul_f32 v[162:163], v[38:39], v[58:59] op_sel_hi:[1,0]
	v_pk_mul_f32 v[160:161], v[34:35], v[58:59] op_sel_hi:[1,0]
	v_max_f32_e32 v34, v163, v60
	v_pk_mul_f32 v[158:159], v[36:37], v[58:59] op_sel_hi:[1,0]
	v_max3_f32 v34, v162, s38, v34
	v_pk_mul_f32 v[156:157], v[48:49], v[58:59] op_sel_hi:[1,0]
	v_pk_mul_f32 v[46:47], v[46:47], v[58:59] op_sel_hi:[1,0]
	v_max_f32_e32 v35, v161, v158
	v_max3_f32 v34, v34, v61, v160
	v_max_f32_e32 v38, v47, v156
	v_max3_f32 v34, v34, v35, v159
	v_pk_mul_f32 v[36:37], v[44:45], v[58:59] op_sel_hi:[1,0]
	v_pk_mul_f32 v[40:41], v[42:43], v[58:59] op_sel_hi:[1,0]
	v_max3_f32 v34, v34, v46, v38
	v_max3_f32 v34, v34, v157, v40
	v_max_f32_e32 v35, v41, v36
	v_max3_f32 v34, v34, v35, v37
	ds_bpermute_b32 v35, v201, v34
	s_waitcnt lgkmcnt(0)
	v_max_f32_e32 v35, v35, v35
	v_max_f32_e32 v34, v34, v35
	ds_bpermute_b32 v35, v202, v34
	s_and_saveexec_b64 s[4:5], vcc
	s_cbranch_execz .LBB0_660
	s_waitcnt lgkmcnt(0)
	v_max_f32_e32 v35, v35, v35
	v_max_f32_e32 v34, v34, v34
	v_max_f32_e32 v34, v34, v35
	ds_write_b32 v165, v34 offset:2304
; __device__ __forceinline__ float row_rms_from_ssq(const float* ssq, int row) {
;     const f32x4* p = (const f32x4*)(ssq + (size_t)row * 16); const f32x4 a = p[0], b = p[1], c = p[2], d = p[3];
;     const float s = (((a[0] + a[1]) + (a[2] + a[3])) + ((b[0] + b[1]) + (b[2] + b[3]))) + (((c[0] + c[1]) + (c[2] + c[3])) + ((d[0] + d[1]) + (d[2] + d[3])));
;     return rsqrtf(s * (1.0f / D) + EPS);
; }
;     __device__ __forceinline__ void operator()(f32x4 (&acc)[2][2][4][2], const pg8::Unit& u, int wr, int wc, int fr, int fq) const {
;         const int row0 = u.pm * 256 + wr * 64 + fr, col0 = u.pn * 256 + wc * 64 + 16 * fq;
; #pragma unroll
;         for (int ai = 0; ai < 2; ++ai)
; #pragma unroll
;             for (int m = 0; m < 4; ++m) { if (m & 1) asm volatile("" ::: "memory");
;                 const float r = row_rms_from_ssq(ssq, row0 + ai * 128 + m * 16) * (1.4426950408889634f / 64.0f);
;                 float mm = -3.0e38f;
; #pragma unroll
;                 for (int bj = 0; bj < 2; ++bj)
; #pragma unroll
;                     for (int n = 0; n < 2; ++n) { acc[ai][bj][m][n] = acc[ai][bj][m][n] * r; const f32x4 v = acc[ai][bj][m][n]; mm = fmaxf(fmaxf(fmaxf(mm, v[0]), fmaxf(v[1], v[2])), v[3]); }
;                 mm = fmaxf(mm, __shfl_xor(mm, 16)); mm = fmaxf(mm, __shfl_xor(mm, 32));
;                 if (fq == 0) xch[(ai * 128 + wr * 64 + m * 16 + fr) * 4 + wc] = mm; }
.LBB0_660:
	s_or_b64 exec, exec, s[4:5]
	v_add_u32_e32 v34, 0xa0, v132
	s_waitcnt lgkmcnt(0)
	v_ashrrev_i32_e32 v35, 31, v34
	v_lshlrev_b64 v[38:39], 6, v[34:35]
	v_lshl_add_u64 v[38:39], s[20:21], 0, v[38:39]
	s_waitcnt vmcnt(4)
	v_mov_b64_e32 v[42:43], v[206:207]
	v_mov_b64_e32 v[44:45], v[208:209]
	v_mov_b64_e32 v[74:75], v[214:215]
	v_mov_b64_e32 v[76:77], v[216:217]
	v_mov_b64_e32 v[166:167], v[210:211]
	v_mov_b64_e32 v[168:169], v[212:213]
	v_mov_b64_e32 v[170:171], v[218:219]
	v_mov_b64_e32 v[172:173], v[220:221]
	v_lshlrev_b32_e32 v205, 4, v164
	v_mov_b32_e32 v38, v42
	v_mov_b32_e32 v39, v74
	v_mov_b32_e32 v74, v43
	v_mov_b32_e32 v42, v44
	v_mov_b32_e32 v43, v76
	v_mov_b32_e32 v76, v45
	v_mov_b32_e32 v44, v166
	v_mov_b32_e32 v45, v170
	v_mov_b32_e32 v170, v167
	v_mov_b32_e32 v48, v168
	v_mov_b32_e32 v49, v172
	v_mov_b32_e32 v172, v169
	v_pk_add_f32 v[38:39], v[38:39], v[74:75]
	v_pk_add_f32 v[42:43], v[42:43], v[76:77]
	v_pk_add_f32 v[44:45], v[44:45], v[170:171]
	v_pk_add_f32 v[48:49], v[48:49], v[172:173]
	v_pk_add_f32 v[38:39], v[38:39], v[42:43]
	v_pk_add_f32 v[42:43], v[44:45], v[48:49]
	s_nop 0
	v_pk_add_f32 v[38:39], v[38:39], v[42:43]
	s_nop 0
	v_add_f32_e32 v38, v38, v39
	v_fmamk_f32 v38, v38, 0x3a800000, v199
	v_mul_f32_e32 v39, 0x4b800000, v38
	v_cmp_gt_f32_e64 s[4:5], s37, v38
	s_nop 1
	v_cndmask_b32_e64 v38, v38, v39, s[4:5]
	v_rsq_f32_e32 v38, v38
	s_nop 0
	v_mul_f32_e32 v39, 0x45800000, v38
	v_cndmask_b32_e64 v38, v38, v39, s[4:5]
	v_mul_f32_e32 v38, 0x3cb8aa3b, v38
	v_pk_mul_f32 v[172:173], v[24:25], v[38:39] op_sel_hi:[1,0]
	v_pk_mul_f32 v[176:177], v[22:23], v[38:39] op_sel_hi:[1,0]
	v_pk_mul_f32 v[168:169], v[18:19], v[38:39] op_sel_hi:[1,0]
	v_max_f32_e32 v18, v177, v172
	v_pk_mul_f32 v[166:167], v[20:21], v[38:39] op_sel_hi:[1,0]
	v_max3_f32 v18, v176, s38, v18
	v_pk_mul_f32 v[32:33], v[32:33], v[38:39] op_sel_hi:[1,0]
	v_pk_mul_f32 v[42:43], v[30:31], v[38:39] op_sel_hi:[1,0]
	v_max_f32_e32 v19, v169, v166
	v_max3_f32 v18, v18, v173, v168
	v_max_f32_e32 v22, v43, v32
	v_max3_f32 v18, v18, v19, v167
	v_pk_mul_f32 v[24:25], v[28:29], v[38:39] op_sel_hi:[1,0]
	v_pk_mul_f32 v[20:21], v[26:27], v[38:39] op_sel_hi:[1,0]
	v_max3_f32 v18, v18, v42, v22
	v_max3_f32 v18, v18, v33, v20
	v_max_f32_e32 v19, v21, v24
	v_max3_f32 v18, v18, v19, v25
	ds_bpermute_b32 v19, v201, v18
	s_waitcnt lgkmcnt(0)
	v_max_f32_e32 v19, v19, v19
	v_max_f32_e32 v18, v18, v19
	ds_bpermute_b32 v19, v202, v18
	s_and_saveexec_b64 s[4:5], s[2:3]
	s_xor_b64 s[2:3], exec, s[4:5]
	v_lshlrev_b32_e32 v205, 4, v164
	s_andn2_saveexec_b64 s[2:3], s[2:3]
	s_cbranch_execz .LBB0_664
	s_waitcnt lgkmcnt(0)
	v_max_f32_e32 v19, v19, v19
	v_max_f32_e32 v18, v18, v18
	v_add_u32_e32 v22, s36, v205
	v_max_f32_e32 v18, v18, v19
	ds_write_b32 v22, v18 offset:2560
.LBB0_664:
	s_or_b64 exec, exec, s[2:3]
	v_add_u32_e32 v18, 0xb0, v132
	s_waitcnt lgkmcnt(0)
	v_ashrrev_i32_e32 v19, 31, v18
	v_lshlrev_b64 v[22:23], 6, v[18:19]
	v_lshl_add_u64 v[22:23], s[20:21], 0, v[22:23]
	s_waitcnt vmcnt(0)
	v_mov_b64_e32 v[26:27], v[222:223]
	v_mov_b64_e32 v[28:29], v[224:225]
	v_mov_b64_e32 v[74:75], v[230:231]
	v_mov_b64_e32 v[76:77], v[232:233]
	v_mov_b64_e32 v[178:179], v[226:227]
	v_mov_b64_e32 v[180:181], v[228:229]
	v_mov_b64_e32 v[182:183], v[234:235]
	v_mov_b64_e32 v[184:185], v[236:237]
	v_mov_b32_e32 v22, v26
	v_mov_b32_e32 v23, v74
	v_mov_b32_e32 v74, v27
	v_mov_b32_e32 v26, v28
	v_mov_b32_e32 v27, v76
	v_mov_b32_e32 v76, v29
	v_mov_b32_e32 v28, v178
	v_mov_b32_e32 v29, v182
	v_mov_b32_e32 v182, v179
	v_mov_b32_e32 v30, v180
	v_mov_b32_e32 v31, v184
	v_mov_b32_e32 v184, v181
	v_pk_add_f32 v[22:23], v[22:23], v[74:75]
	v_pk_add_f32 v[26:27], v[26:27], v[76:77]
	v_pk_add_f32 v[28:29], v[28:29], v[182:183]
	v_pk_add_f32 v[30:31], v[30:31], v[184:185]
	v_pk_add_f32 v[22:23], v[22:23], v[26:27]
	v_pk_add_f32 v[26:27], v[28:29], v[30:31]
	s_nop 0
	v_pk_add_f32 v[22:23], v[22:23], v[26:27]
	s_nop 0
	v_add_f32_e32 v22, v22, v23
	v_fmamk_f32 v22, v22, 0x3a800000, v199
	v_mul_f32_e32 v23, 0x4b800000, v22
	v_cmp_gt_f32_e64 s[2:3], s37, v22
	s_nop 1
	v_cndmask_b32_e64 v22, v22, v23, s[2:3]
	v_rsq_f32_e32 v22, v22
	s_nop 0
	v_mul_f32_e32 v23, 0x45800000, v22
	v_cndmask_b32_e64 v22, v22, v23, s[2:3]
	v_mul_f32_e32 v22, 0x3cb8aa3b, v22
	v_pk_mul_f32 v[190:191], v[8:9], v[22:23] op_sel_hi:[1,0]
	v_pk_mul_f32 v[192:193], v[6:7], v[22:23] op_sel_hi:[1,0]
	v_pk_mul_f32 v[188:189], v[2:3], v[22:23] op_sel_hi:[1,0]
	v_max_f32_e32 v2, v193, v190
	v_pk_mul_f32 v[186:187], v[4:5], v[22:23] op_sel_hi:[1,0]
	v_max3_f32 v2, v192, s38, v2
	v_pk_mul_f32 v[182:183], v[16:17], v[22:23] op_sel_hi:[1,0]
	v_pk_mul_f32 v[184:185], v[14:15], v[22:23] op_sel_hi:[1,0]
	v_max_f32_e32 v3, v189, v186
	v_max3_f32 v2, v2, v191, v188
	v_max_f32_e32 v4, v185, v182
	v_max3_f32 v2, v2, v3, v187
	v_pk_mul_f32 v[178:179], v[12:13], v[22:23] op_sel_hi:[1,0]
	v_pk_mul_f32 v[180:181], v[10:11], v[22:23] op_sel_hi:[1,0]
	v_max3_f32 v2, v2, v184, v4
	v_max3_f32 v2, v2, v183, v180
	v_max_f32_e32 v3, v181, v178
	v_max3_f32 v2, v2, v3, v179
	ds_bpermute_b32 v3, v201, v2
	s_waitcnt lgkmcnt(0)
	v_max_f32_e32 v3, v3, v3
	v_max_f32_e32 v2, v2, v3
	ds_bpermute_b32 v3, v202, v2
	s_and_saveexec_b64 s[2:3], vcc
	s_cbranch_execz .LBB0_666
	s_waitcnt lgkmcnt(0)
	v_max_f32_e32 v3, v3, v3
	v_max_f32_e32 v2, v2, v2
	v_add_u32_e32 v4, s36, v205
	v_max_f32_e32 v2, v2, v3
	ds_write_b32 v4, v2 offset:2816
